# attention key loop: no VALU in the first four MFMA gaps after the tile barrier (row-sum adds in the last two gaps of the S0 chain) (v33 otherwise)
# baseline (speedup 1.0000x reference)
.Lfa_noload_0:
	ds_read_b128 v[114:117], v130 offset:64
	ds_read_b128 v[118:121], v130 offset:96
	ds_read_b128 v[122:125], v130 offset:128
	ds_read_b128 v[132:135], v130 offset:160
	ds_read_b128 v[136:139], v130 offset:192
	ds_read_b128 v[140:143], v130 offset:224
	ds_read_b128 v[146:149], v130 offset:6720
	ds_read_b128 v[150:153], v130 offset:6752
	s_waitcnt lgkmcnt(7)
	v_mfma_f32_32x32x16_bf16 v[34:49], v[114:117], v[86:89], 0
	ds_read_b128 v[154:157], v130 offset:6784
	s_waitcnt lgkmcnt(7)
	v_mfma_f32_32x32x16_bf16 v[34:49], v[118:121], v[82:85], v[34:49]
	ds_read_b128 v[158:161], v130 offset:6816
	s_waitcnt lgkmcnt(7)
	v_mfma_f32_32x32x16_bf16 v[34:49], v[122:125], v[78:81], v[34:49]
	ds_read_b128 v[162:165], v130 offset:6848
	s_waitcnt lgkmcnt(7)
	v_mfma_f32_32x32x16_bf16 v[34:49], v[132:135], v[74:77], v[34:49]
	ds_read_b128 v[166:169], v130 offset:6880
	s_waitcnt lgkmcnt(7)
	v_mfma_f32_32x32x16_bf16 v[34:49], v[136:139], v[70:73], v[34:49]
	v_add_f32_e32 v105, v105, v50
	v_add_f32_e32 v145, v145, v51
	v_add_f32_e32 v105, v105, v52
	v_add_f32_e32 v145, v145, v53
	v_add_f32_e32 v105, v105, v54
	v_add_f32_e32 v145, v145, v55
	v_add_f32_e32 v105, v105, v56
	v_add_f32_e32 v145, v145, v57
	s_waitcnt lgkmcnt(6)
	v_mfma_f32_32x32x16_bf16 v[34:49], v[140:143], v[66:69], v[34:49]
	v_add_f32_e32 v105, v105, v58
	v_add_f32_e32 v145, v145, v59
	v_add_f32_e32 v105, v105, v60
	v_add_f32_e32 v145, v145, v61
	v_add_f32_e32 v105, v105, v62
	v_add_f32_e32 v145, v145, v63
	v_add_f32_e32 v105, v105, v64
	v_add_f32_e32 v145, v145, v65
	s_waitcnt lgkmcnt(5)
	v_mfma_f32_32x32x16_bf16 v[50:65], v[146:149], v[86:89], 0
	ds_read_b128 v[114:117], v107 offset:13376
	ds_read_b128 v[118:121], v107 offset:17984
	ds_read_b128 v[122:125], v107 offset:13408
	ds_read_b128 v[132:135], v107 offset:18016
	ds_read_b128 v[136:139], v107 offset:13440
	ds_read_b128 v[140:143], v107 offset:18048
	ds_read_b128 v[146:149], v107 offset:13472
	s_waitcnt lgkmcnt(11)
	v_mfma_f32_32x32x16_bf16 v[50:65], v[150:153], v[82:85], v[50:65]
	ds_read_b128 v[150:153], v107 offset:18080
	v_lshl_add_u64 v[112:113], v[112:113], 0, s[12:13]
	v_lshl_add_u64 v[110:111], v[110:111], 0, v[194:195]
	v_lshl_add_u64 v[108:109], v[108:109], 0, s[10:11]
	v_exp_f32_e32 v34, v34
	v_exp_f32_e32 v35, v35
	s_waitcnt lgkmcnt(11)
	v_mfma_f32_32x32x16_bf16 v[50:65], v[154:157], v[78:81], v[50:65]
	v_exp_f32_e32 v36, v36
	v_exp_f32_e32 v37, v37
	v_exp_f32_e32 v38, v38
	s_waitcnt lgkmcnt(10)
	v_mfma_f32_32x32x16_bf16 v[50:65], v[158:161], v[74:77], v[50:65]
	v_exp_f32_e32 v39, v39
	v_exp_f32_e32 v40, v40
	v_exp_f32_e32 v41, v41
	v_cvt_pk_bf16_f32 v154, v34, v35
	s_waitcnt lgkmcnt(9)
	v_mfma_f32_32x32x16_bf16 v[50:65], v[162:165], v[70:73], v[50:65]
	v_cvt_pk_bf16_f32 v155, v36, v37
	v_cvt_pk_bf16_f32 v156, v38, v39
	v_exp_f32_e32 v42, v42
	v_exp_f32_e32 v43, v43
	s_waitcnt lgkmcnt(8)
	v_mfma_f32_32x32x16_bf16 v[50:65], v[166:169], v[66:69], v[50:65]
	v_cvt_pk_bf16_f32 v157, v40, v41
	v_exp_f32_e32 v44, v44
	v_exp_f32_e32 v45, v45
	v_exp_f32_e32 v46, v46
	s_waitcnt lgkmcnt(7)
	v_mfma_f32_32x32x16_bf16 v[18:33], v[114:117], v[154:157], v[18:33]
	v_exp_f32_e32 v47, v47
	v_exp_f32_e32 v48, v48
	v_exp_f32_e32 v49, v49
	v_cvt_pk_bf16_f32 v158, v42, v43
	s_waitcnt lgkmcnt(6)
	v_mfma_f32_32x32x16_bf16 v[2:17], v[118:121], v[154:157], v[2:17]
	v_cvt_pk_bf16_f32 v159, v44, v45
	v_cvt_pk_bf16_f32 v160, v46, v47
	v_cvt_pk_bf16_f32 v161, v48, v49
	v_add_f32_e32 v105, v105, v34
	v_add_f32_e32 v145, v145, v35
	v_add_f32_e32 v105, v105, v36
	v_exp_f32_e32 v50, v50
	s_waitcnt lgkmcnt(5)
	v_mfma_f32_32x32x16_bf16 v[18:33], v[122:125], v[158:161], v[18:33]
	v_exp_f32_e32 v51, v51
	v_exp_f32_e32 v52, v52
	v_exp_f32_e32 v53, v53
	s_waitcnt lgkmcnt(4)
	v_mfma_f32_32x32x16_bf16 v[2:17], v[132:135], v[158:161], v[2:17]
	v_exp_f32_e32 v54, v54
	v_exp_f32_e32 v55, v55
	v_exp_f32_e32 v56, v56
	v_exp_f32_e32 v57, v57
	v_cvt_pk_bf16_f32 v162, v50, v51
	v_cvt_pk_bf16_f32 v163, v52, v53
	v_cvt_pk_bf16_f32 v164, v54, v55
	v_cvt_pk_bf16_f32 v165, v56, v57
	v_add_f32_e32 v145, v145, v37
	v_add_f32_e32 v105, v105, v38
	s_waitcnt lgkmcnt(3)
	v_mfma_f32_32x32x16_bf16 v[18:33], v[136:139], v[162:165], v[18:33]
	v_exp_f32_e32 v58, v58
	v_exp_f32_e32 v59, v59
	v_exp_f32_e32 v60, v60
	s_waitcnt lgkmcnt(2)
	v_mfma_f32_32x32x16_bf16 v[2:17], v[140:143], v[162:165], v[2:17]
	v_exp_f32_e32 v61, v61
	v_exp_f32_e32 v62, v62
	v_exp_f32_e32 v63, v63
	v_exp_f32_e32 v64, v64
	v_exp_f32_e32 v65, v65
	v_cvt_pk_bf16_f32 v166, v58, v59
	v_cvt_pk_bf16_f32 v167, v60, v61
	v_cvt_pk_bf16_f32 v168, v62, v63
	v_cvt_pk_bf16_f32 v169, v64, v65
	v_add_f32_e32 v145, v145, v39
	v_add_f32_e32 v105, v105, v40
	s_waitcnt lgkmcnt(1)
	v_mfma_f32_32x32x16_bf16 v[18:33], v[146:149], v[166:169], v[18:33]
	v_add_f32_e32 v145, v145, v41
	v_add_f32_e32 v105, v105, v42
	v_add_f32_e32 v145, v145, v43
	v_add_f32_e32 v105, v105, v44
	v_add_f32_e32 v145, v145, v45
	s_waitcnt lgkmcnt(0)
	v_mfma_f32_32x32x16_bf16 v[2:17], v[150:153], v[166:169], v[2:17]
	v_add_f32_e32 v105, v105, v46
	v_add_f32_e32 v145, v145, v47
	v_add_f32_e32 v105, v105, v48
	v_add_f32_e32 v145, v145, v49
	s_cmp_lt_u32 s31, s65
	s_cbranch_scc0 .Lfa_nowrite_0
	s_waitcnt vmcnt(0)
	ds_write_b128 v106, v[98:101] offset:22592
	ds_write_b128 v128, v[94:97] offset:22592
	s_cmp_lg_u32 s43, 0
	s_cbranch_scc0 .Lfa_nowrite_0
	ds_write_b128 v129, v[90:93] offset:35904

.Lfa_noload_1:
	ds_read_b128 v[114:117], v130 offset:22592
	ds_read_b128 v[118:121], v130 offset:22624
	ds_read_b128 v[122:125], v130 offset:22656
	ds_read_b128 v[132:135], v130 offset:22688
	ds_read_b128 v[136:139], v130 offset:22720
	ds_read_b128 v[140:143], v130 offset:22752
	ds_read_b128 v[146:149], v130 offset:29248
	ds_read_b128 v[150:153], v130 offset:29280
	s_waitcnt lgkmcnt(7)
	v_mfma_f32_32x32x16_bf16 v[34:49], v[114:117], v[86:89], 0
	ds_read_b128 v[154:157], v130 offset:29312
	s_waitcnt lgkmcnt(7)
	v_mfma_f32_32x32x16_bf16 v[34:49], v[118:121], v[82:85], v[34:49]
	ds_read_b128 v[158:161], v130 offset:29344
	s_waitcnt lgkmcnt(7)
	v_mfma_f32_32x32x16_bf16 v[34:49], v[122:125], v[78:81], v[34:49]
	ds_read_b128 v[162:165], v130 offset:29376
	s_waitcnt lgkmcnt(7)
	v_mfma_f32_32x32x16_bf16 v[34:49], v[132:135], v[74:77], v[34:49]
	ds_read_b128 v[166:169], v130 offset:29408
	s_waitcnt lgkmcnt(7)
	v_mfma_f32_32x32x16_bf16 v[34:49], v[136:139], v[70:73], v[34:49]
	v_add_f32_e32 v105, v105, v50
	v_add_f32_e32 v145, v145, v51
	v_add_f32_e32 v105, v105, v52
	v_add_f32_e32 v145, v145, v53
	v_add_f32_e32 v105, v105, v54
	v_add_f32_e32 v145, v145, v55
	v_add_f32_e32 v105, v105, v56
	v_add_f32_e32 v145, v145, v57
	s_waitcnt lgkmcnt(6)
	v_mfma_f32_32x32x16_bf16 v[34:49], v[140:143], v[66:69], v[34:49]
	v_add_f32_e32 v105, v105, v58
	v_add_f32_e32 v145, v145, v59
	v_add_f32_e32 v105, v105, v60
	v_add_f32_e32 v145, v145, v61
	v_add_f32_e32 v105, v105, v62
	v_add_f32_e32 v145, v145, v63
	v_add_f32_e32 v105, v105, v64
	v_add_f32_e32 v145, v145, v65
	s_waitcnt lgkmcnt(5)
	v_mfma_f32_32x32x16_bf16 v[50:65], v[146:149], v[86:89], 0
	ds_read_b128 v[114:117], v107 offset:35904
	ds_read_b128 v[118:121], v107 offset:40512
	ds_read_b128 v[122:125], v107 offset:35936
	ds_read_b128 v[132:135], v107 offset:40544
	ds_read_b128 v[136:139], v107 offset:35968
	ds_read_b128 v[140:143], v107 offset:40576
	ds_read_b128 v[146:149], v107 offset:36000
	s_waitcnt lgkmcnt(11)
	v_mfma_f32_32x32x16_bf16 v[50:65], v[150:153], v[82:85], v[50:65]
	ds_read_b128 v[150:153], v107 offset:40608
	v_lshl_add_u64 v[112:113], v[112:113], 0, s[12:13]
	v_lshl_add_u64 v[110:111], v[110:111], 0, v[194:195]
	v_lshl_add_u64 v[108:109], v[108:109], 0, s[10:11]
	v_exp_f32_e32 v34, v34
	v_exp_f32_e32 v35, v35
	s_waitcnt lgkmcnt(11)
	v_mfma_f32_32x32x16_bf16 v[50:65], v[154:157], v[78:81], v[50:65]
	v_exp_f32_e32 v36, v36
	v_exp_f32_e32 v37, v37
	v_exp_f32_e32 v38, v38
	s_waitcnt lgkmcnt(10)
	v_mfma_f32_32x32x16_bf16 v[50:65], v[158:161], v[74:77], v[50:65]
	v_exp_f32_e32 v39, v39
	v_exp_f32_e32 v40, v40
	v_exp_f32_e32 v41, v41
	v_cvt_pk_bf16_f32 v154, v34, v35
	s_waitcnt lgkmcnt(9)
	v_mfma_f32_32x32x16_bf16 v[50:65], v[162:165], v[70:73], v[50:65]
	v_cvt_pk_bf16_f32 v155, v36, v37
	v_cvt_pk_bf16_f32 v156, v38, v39
	v_exp_f32_e32 v42, v42
	v_exp_f32_e32 v43, v43
	s_waitcnt lgkmcnt(8)
	v_mfma_f32_32x32x16_bf16 v[50:65], v[166:169], v[66:69], v[50:65]
	v_cvt_pk_bf16_f32 v157, v40, v41
	v_exp_f32_e32 v44, v44
	v_exp_f32_e32 v45, v45
	v_exp_f32_e32 v46, v46
	s_waitcnt lgkmcnt(7)
	v_mfma_f32_32x32x16_bf16 v[18:33], v[114:117], v[154:157], v[18:33]
	v_exp_f32_e32 v47, v47
	v_exp_f32_e32 v48, v48
	v_exp_f32_e32 v49, v49
	v_cvt_pk_bf16_f32 v158, v42, v43
	s_waitcnt lgkmcnt(6)
	v_mfma_f32_32x32x16_bf16 v[2:17], v[118:121], v[154:157], v[2:17]
	v_cvt_pk_bf16_f32 v159, v44, v45
	v_cvt_pk_bf16_f32 v160, v46, v47
	v_cvt_pk_bf16_f32 v161, v48, v49
	v_add_f32_e32 v105, v105, v34
	v_add_f32_e32 v145, v145, v35
	v_add_f32_e32 v105, v105, v36
	v_exp_f32_e32 v50, v50
	s_waitcnt lgkmcnt(5)
	v_mfma_f32_32x32x16_bf16 v[18:33], v[122:125], v[158:161], v[18:33]
	v_exp_f32_e32 v51, v51
	v_exp_f32_e32 v52, v52
	v_exp_f32_e32 v53, v53
	s_waitcnt lgkmcnt(4)
	v_mfma_f32_32x32x16_bf16 v[2:17], v[132:135], v[158:161], v[2:17]
	v_exp_f32_e32 v54, v54
	v_exp_f32_e32 v55, v55
	v_exp_f32_e32 v56, v56
	v_exp_f32_e32 v57, v57
	v_cvt_pk_bf16_f32 v162, v50, v51
	v_cvt_pk_bf16_f32 v163, v52, v53
	v_cvt_pk_bf16_f32 v164, v54, v55
	v_cvt_pk_bf16_f32 v165, v56, v57
	v_add_f32_e32 v145, v145, v37
	v_add_f32_e32 v105, v105, v38
	s_waitcnt lgkmcnt(3)
	v_mfma_f32_32x32x16_bf16 v[18:33], v[136:139], v[162:165], v[18:33]
	v_exp_f32_e32 v58, v58
	v_exp_f32_e32 v59, v59
	v_exp_f32_e32 v60, v60
	s_waitcnt lgkmcnt(2)
	v_mfma_f32_32x32x16_bf16 v[2:17], v[140:143], v[162:165], v[2:17]
	v_exp_f32_e32 v61, v61
	v_exp_f32_e32 v62, v62
	v_exp_f32_e32 v63, v63
	v_exp_f32_e32 v64, v64
	v_exp_f32_e32 v65, v65
	v_cvt_pk_bf16_f32 v166, v58, v59
	v_cvt_pk_bf16_f32 v167, v60, v61
	v_cvt_pk_bf16_f32 v168, v62, v63
	v_cvt_pk_bf16_f32 v169, v64, v65
	v_add_f32_e32 v145, v145, v39
	v_add_f32_e32 v105, v105, v40
	s_waitcnt lgkmcnt(1)
	v_mfma_f32_32x32x16_bf16 v[18:33], v[146:149], v[166:169], v[18:33]
	v_add_f32_e32 v145, v145, v41
	v_add_f32_e32 v105, v105, v42
	v_add_f32_e32 v145, v145, v43
	v_add_f32_e32 v105, v105, v44
	v_add_f32_e32 v145, v145, v45
	s_waitcnt lgkmcnt(0)
	v_mfma_f32_32x32x16_bf16 v[2:17], v[150:153], v[166:169], v[2:17]
	v_add_f32_e32 v105, v105, v46
	v_add_f32_e32 v145, v145, v47
	v_add_f32_e32 v105, v105, v48
	v_add_f32_e32 v145, v145, v49
	s_cmp_lt_u32 s31, s65
	s_cbranch_scc0 .Lfa_nowrite_1
	s_waitcnt vmcnt(0)
	ds_write_b128 v106, v[98:101] offset:64
	ds_write_b128 v128, v[94:97] offset:64
	s_cmp_lg_u32 s43, 0
	s_cbranch_scc0 .Lfa_nowrite_1
	ds_write_b128 v129, v[90:93] offset:13376
